# baseline (speedup 1.0000x reference)
.LBB1_2:
	s_or_b64 exec, exec, s[4:5]
	v_lshl_or_b32 v8, s2, 3, v8
	v_mov_b32_e32 v151, 0
	v_readfirstlane_b32 s4, v8
	s_ashr_i32 s5, s4, 31
	s_lshl_b64 s[4:5], s[4:5], 2
	s_add_u32 s8, s8, s4
	v_add_u32_e32 v172, 0x22c00, v2
	s_addc_u32 s9, s9, s5
	v_lshl_add_u32 v173, v1, 2, v172
	s_add_u32 s4, s10, s4
	ds_write_b32 v173, v151
	s_addc_u32 s5, s11, s5
	s_load_dword s12, s[6:7], 0x4000
	s_load_dword s19, s[8:9], 0x0
	v_lshrrev_b32_e32 v18, 5, v1
	s_load_dword s3, s[4:5], 0x0
	s_movk_i32 s4, 0xff
	v_cmp_lt_u32_e32 vcc, s4, v0
	v_bfe_u32 v64, v0, 6, 1
	v_lshlrev_b32_e32 v174, 4, v18
	s_waitcnt vmcnt(8)
	s_barrier
	s_and_saveexec_b64 s[4:5], vcc
	s_xor_b64 s[4:5], exec, s[4:5]
	s_cbranch_execz .LBB1_6
	v_lshlrev_b32_e32 v2, 2, v0
	v_and_b32_e32 v2, 0x7c, v2
	v_bfe_u32 v19, v0, 7, 1
	v_lshl_or_b32 v2, v64, 7, v2
	v_lshl_or_b32 v32, v19, 12, v150
	ds_read_b32 v2, v2 offset:35584
	ds_read_b128 v[20:23], v32
	v_lshlrev_b32_e32 v40, 12, v64
	v_or_b32_e32 v41, v40, v150
	ds_read_b128 v[24:27], v41 offset:24576
	ds_read_b128 v[28:31], v32 offset:3072
	s_waitcnt lgkmcnt(3)
	v_mov_b32_e32 v3, v2
	v_mov_b32_e32 v4, v2
	v_mov_b32_e32 v5, v2
	v_mov_b32_e32 v6, v2
	v_mov_b32_e32 v7, v2
	v_mov_b32_e32 v8, v2
	v_mov_b32_e32 v9, v2
	v_mov_b32_e32 v10, v2
	v_mov_b32_e32 v11, v2
	v_mov_b32_e32 v12, v2
	v_mov_b32_e32 v13, v2
	v_mov_b32_e32 v14, v2
	v_mov_b32_e32 v15, v2
	v_mov_b32_e32 v16, v2
	v_mov_b32_e32 v17, v2
	v_lshlrev_b32_e32 v19, 11, v19
	v_or3_b32 v19, v19, v40, v150
	s_waitcnt lgkmcnt(1)
	v_mfma_f32_32x32x16_bf16 v[2:17], v[20:23], v[24:27], v[2:17]
	ds_read_b128 v[20:23], v32 offset:1024
	ds_read_b128 v[24:27], v41 offset:25600
	ds_read_b128 v[32:35], v32 offset:2048
	ds_read_b128 v[36:39], v41 offset:26624
	v_add_u32_e32 v19, 0x20c00, v19
	s_waitcnt lgkmcnt(2)
	v_mfma_f32_32x32x16_bf16 v[2:17], v[20:23], v[24:27], v[2:17]
	ds_read_b128 v[20:23], v41 offset:27648
	s_waitcnt lgkmcnt(1)
	v_mfma_f32_32x32x16_bf16 v[2:17], v[32:35], v[36:39], v[2:17]
	s_waitcnt lgkmcnt(0)
	v_mfma_f32_32x32x16_bf16 v[2:17], v[28:31], v[20:23], v[2:17]
	s_nop 11
	v_cvt_pk_bf16_f32 v9, v8, v9
	v_cvt_pk_bf16_f32 v8, v6, v7
	v_cvt_pk_bf16_f32 v7, v4, v5
	v_cvt_pk_bf16_f32 v6, v2, v3
	v_cvt_pk_bf16_f32 v5, v16, v17
	v_cvt_pk_bf16_f32 v4, v14, v15
	v_cvt_pk_bf16_f32 v3, v12, v13
	v_cvt_pk_bf16_f32 v2, v10, v11
	ds_write_b128 v19, v[6:9]
	ds_write_b128 v19, v[2:5] offset:1024
	v_lshlrev_b32_e32 v2, 4, v18

.LBB1_8:
	s_or_b64 exec, exec, s[4:5]
	s_waitcnt vmcnt(0) lgkmcnt(0)
	v_lshl_or_b32 v186, s19, 6, v1
	v_ashrrev_i32_e32 v187, 31, v186
	v_lshl_add_u64 v[186:187], v[186:187], 2, s[6:7]
	global_load_dword v175, v[186:187], off
	v_mov_b32_e32 v184, 1
	v_lshl_add_u32 v180, v176, 2, v172
	v_lshl_add_u32 v181, v177, 2, v172
	v_lshl_add_u32 v182, v178, 2, v172
	v_lshl_add_u32 v183, v179, 2, v172
	s_waitcnt lgkmcnt(0)
	ds_add_u32 v180, v184
	ds_add_u32 v181, v184
	ds_add_u32 v182, v184
	ds_add_u32 v183, v184
	s_waitcnt lgkmcnt(0)
	ds_read_b32 v151, v173
	s_waitcnt lgkmcnt(0)
	v_cvt_f32_i32_e32 v185, v151
	ds_write_b32 v173, v185 offset:256
	v_add_u32_e32 v10, v172, v2
	s_waitcnt vmcnt(1) lgkmcnt(0)
	s_barrier
	s_nop 0
	ds_read_b128 v[18:21], v10 offset:256
	ds_read_b128 v[22:25], v10 offset:288
	ds_read_b128 v[82:85], v10 offset:320
	ds_read_b128 v[86:89], v10 offset:352
	ds_read_b128 v[74:77], v10 offset:384
	ds_read_b128 v[78:81], v10 offset:416
	ds_read_b128 v[2:5], v213 offset:32768
	ds_read_b128 v[6:9], v213 offset:0
	ds_read_b128 v[66:69], v10 offset:448
	ds_read_b128 v[70:73], v10 offset:480
	ds_read_b128 v[10:13], v213 offset:1024
	s_waitcnt lgkmcnt(3)
	v_pk_mul_f32 v[26:27], v[8:9], v[20:21]
	v_pk_mul_f32 v[28:29], v[6:7], v[18:19]
	ds_read_b128 v[14:17], v213 offset:8192
	s_waitcnt lgkmcnt(1)
	v_pk_mul_f32 v[12:13], v[12:13], v[24:25]
	v_pk_mul_f32 v[10:11], v[10:11], v[22:23]
	v_pk_fma_f32 v[30:31], v[8:9], v[20:21], v[12:13]
	v_pk_fma_f32 v[32:33], v[6:7], v[18:19], v[10:11]
	v_cvt_pk_bf16_f32 v9, v12, v13
	v_cvt_pk_bf16_f32 v7, v26, v27
	v_cvt_pk_bf16_f32 v8, v10, v11
	v_cvt_pk_bf16_f32 v6, v28, v29
	ds_read_b128 v[10:13], v213 offset:33792
	s_nop 0
	v_mfma_f32_32x32x16_bf16 v[34:49], v[2:5], v[6:9], 0
	ds_read_b128 v[6:9], v213 offset:9216
	s_waitcnt lgkmcnt(2)
	v_mul_f32_e32 v26, v16, v20
	v_mul_f32_e32 v27, v17, v21
	v_pk_mul_f32 v[50:51], v[14:15], v[18:19]
	s_mov_b32 s4, 0x3727c5ac
	s_waitcnt lgkmcnt(0)
	v_pk_mul_f32 v[8:9], v[8:9], v[24:25]
	v_pk_mul_f32 v[28:29], v[6:7], v[22:23]
	v_pk_fma_f32 v[90:91], v[16:17], v[20:21], v[8:9]
	v_pk_fma_f32 v[92:93], v[14:15], v[18:19], v[28:29]
	ds_read_b128 v[14:17], v213 offset:2048
	v_cvt_pk_bf16_f32 v9, v8, v9
	v_cvt_pk_bf16_f32 v7, v26, v27
	v_cvt_pk_bf16_f32 v8, v28, v29
	ds_read_b128 v[26:29], v213 offset:3072
	v_cvt_pk_bf16_f32 v6, v50, v51
	s_waitcnt lgkmcnt(1)
	v_pk_mul_f32 v[94:95], v[14:15], v[82:83]
	s_mov_b32 s0, 0x3c800000
	v_mfma_f32_32x32x16_bf16 v[50:65], v[2:5], v[6:9], 0
	v_mul_f32_e32 v2, v16, v84
	v_mul_f32_e32 v3, v17, v85
	s_waitcnt lgkmcnt(0)
	v_mul_f32_e32 v4, v28, v88
	v_mul_f32_e32 v5, v29, v89
	v_pk_mul_f32 v[6:7], v[26:27], v[86:87]
	v_pk_fma_f32 v[8:9], v[16:17], v[84:85], v[4:5]
	v_cvt_pk_bf16_f32 v3, v2, v3
	v_pk_fma_f32 v[14:15], v[14:15], v[82:83], v[6:7]
	v_pk_add_f32 v[26:27], v[8:9], v[30:31]
	v_cvt_pk_bf16_f32 v5, v4, v5
	v_cvt_pk_bf16_f32 v4, v6, v7
	ds_read_b128 v[6:9], v213 offset:10240
	v_pk_add_f32 v[28:29], v[14:15], v[32:33]
	ds_read_b128 v[14:17], v213 offset:11264
	v_cvt_pk_bf16_f32 v2, v94, v95
	s_waitcnt lgkmcnt(1)
	v_pk_mul_f32 v[30:31], v[6:7], v[82:83]
	v_mov_b64_e32 v[152:153], s[4:5]
	v_mfma_f32_32x32x16_bf16 v[34:49], v[10:13], v[2:5], v[34:49]
	v_mul_f32_e32 v2, v8, v84
	v_mul_f32_e32 v3, v9, v85
	s_waitcnt lgkmcnt(0)
	v_mul_f32_e32 v4, v16, v88
	v_mul_f32_e32 v5, v17, v89
	v_pk_mul_f32 v[14:15], v[14:15], v[86:87]
	v_pk_fma_f32 v[8:9], v[8:9], v[84:85], v[4:5]
	v_pk_fma_f32 v[6:7], v[6:7], v[82:83], v[14:15]
	v_cvt_pk_bf16_f32 v5, v4, v5
	v_cvt_pk_bf16_f32 v3, v2, v3
	v_cvt_pk_bf16_f32 v4, v14, v15
	v_pk_add_f32 v[32:33], v[8:9], v[90:91]
	v_pk_add_f32 v[90:91], v[6:7], v[92:93]
	ds_read_b128 v[6:9], v213 offset:34816
	ds_read_b128 v[14:17], v213 offset:4096
	v_cvt_pk_bf16_f32 v2, v30, v31
	s_mov_b32 s13, 0
	s_mov_b64 s[6:7], 0
	v_mfma_f32_32x32x16_bf16 v[50:65], v[10:13], v[2:5], v[50:65]
	ds_read_b128 v[2:5], v213 offset:5120
	ds_read_b128 v[10:13], v213 offset:12288
	s_waitcnt lgkmcnt(2)
	v_pk_mul_f32 v[30:31], v[16:17], v[76:77]
	v_pk_mul_f32 v[92:93], v[14:15], v[74:75]
	s_waitcnt lgkmcnt(1)
	v_pk_mul_f32 v[4:5], v[4:5], v[80:81]
	v_pk_mul_f32 v[94:95], v[2:3], v[78:79]
	v_pk_fma_f32 v[2:3], v[16:17], v[76:77], v[4:5]
	v_cvt_pk_bf16_f32 v5, v4, v5
	v_pk_add_f32 v[96:97], v[2:3], v[26:27]
	v_cvt_pk_bf16_f32 v3, v30, v31
	v_cvt_pk_bf16_f32 v4, v94, v95
	v_cvt_pk_bf16_f32 v2, v92, v93
	v_pk_fma_f32 v[14:15], v[14:15], v[74:75], v[94:95]
	s_waitcnt lgkmcnt(0)
	v_pk_mul_f32 v[30:31], v[10:11], v[74:75]
	v_mfma_f32_32x32x16_bf16 v[34:49], v[6:9], v[2:5], v[34:49]
	ds_read_b128 v[2:5], v213 offset:13312
	v_add_f32_e32 v98, v14, v28
	v_add_f32_e32 v99, v15, v29
	ds_read_b128 v[14:17], v213 offset:35840
	v_pk_mul_f32 v[26:27], v[12:13], v[76:77]
	s_waitcnt lgkmcnt(1)
	v_pk_mul_f32 v[4:5], v[4:5], v[80:81]
	v_pk_mul_f32 v[28:29], v[2:3], v[78:79]
	v_pk_fma_f32 v[2:3], v[12:13], v[76:77], v[4:5]
	v_pk_fma_f32 v[10:11], v[10:11], v[74:75], v[28:29]
	v_pk_add_f32 v[32:33], v[2:3], v[32:33]
	v_pk_add_f32 v[92:93], v[10:11], v[90:91]
	ds_read_b128 v[10:13], v213 offset:6144
	v_cvt_pk_bf16_f32 v5, v4, v5
	v_cvt_pk_bf16_f32 v3, v26, v27
	v_cvt_pk_bf16_f32 v4, v28, v29
	ds_read_b128 v[26:29], v213 offset:7168
	v_cvt_pk_bf16_f32 v2, v30, v31
	s_waitcnt lgkmcnt(1)
	v_pk_mul_f32 v[30:31], v[10:11], v[66:67]
	v_mfma_f32_32x32x16_bf16 v[50:65], v[6:9], v[2:5], v[50:65]
	v_mul_f32_e32 v2, v12, v68
	v_mul_f32_e32 v3, v13, v69
	s_waitcnt lgkmcnt(0)
	v_mul_f32_e32 v4, v28, v72
	v_mul_f32_e32 v5, v29, v73
	v_pk_mul_f32 v[6:7], v[26:27], v[70:71]
	v_pk_fma_f32 v[8:9], v[12:13], v[68:69], v[4:5]
	v_cvt_pk_bf16_f32 v3, v2, v3
	v_pk_fma_f32 v[10:11], v[10:11], v[66:67], v[6:7]
	v_pk_add_f32 v[94:95], v[8:9], v[96:97]
	v_cvt_pk_bf16_f32 v5, v4, v5
	v_cvt_pk_bf16_f32 v4, v6, v7
	ds_read_b128 v[6:9], v213 offset:14336
	v_pk_add_f32 v[96:97], v[10:11], v[98:99]
	ds_read_b128 v[10:13], v213 offset:15360
	v_cvt_pk_bf16_f32 v2, v30, v31
	s_waitcnt lgkmcnt(1)
	v_pk_mul_f32 v[30:31], v[6:7], v[66:67]
	v_mfma_f32_32x32x16_bf16 v[34:49], v[14:17], v[2:5], v[34:49]
	s_waitcnt lgkmcnt(0)
	v_mul_f32_e32 v10, v10, v70
	v_mul_f32_e32 v11, v11, v71
	v_mul_f32_e32 v2, v8, v68
	v_mul_f32_e32 v3, v9, v69
	v_pk_mul_f32 v[4:5], v[12:13], v[72:73]
	v_pk_fma_f32 v[6:7], v[6:7], v[66:67], v[10:11]
	v_pk_fma_f32 v[8:9], v[8:9], v[68:69], v[4:5]
	v_pk_add_f32 v[92:93], v[6:7], v[92:93]
	v_cvt_pk_bf16_f32 v3, v2, v3
	v_pk_add_f32 v[90:91], v[8:9], v[32:33]
	v_cvt_pk_bf16_f32 v5, v4, v5
	v_cvt_pk_bf16_f32 v4, v10, v11
	ds_read_b128 v[26:29], v213 offset:36864
	ds_read_b128 v[6:9], v213 offset:16384
	v_cvt_pk_bf16_f32 v2, v30, v31
	ds_read_b128 v[98:101], v213 offset:25600
	ds_read_b128 v[102:105], v213 offset:37888
	v_mfma_f32_32x32x16_bf16 v[50:65], v[14:17], v[2:5], v[50:65]
	ds_read_b128 v[2:5], v213 offset:17408
	ds_read_b128 v[30:33], v213 offset:24576
	s_waitcnt lgkmcnt(4)
	v_pk_mul_f32 v[12:13], v[6:7], v[18:19]
	v_pk_mul_f32 v[10:11], v[8:9], v[20:21]
	s_waitcnt lgkmcnt(1)
	v_pk_mul_f32 v[14:15], v[2:3], v[22:23]
	v_pk_mul_f32 v[22:23], v[98:99], v[22:23]
	v_pk_fma_f32 v[112:113], v[6:7], v[18:19], v[14:15]
	s_waitcnt lgkmcnt(0)
	v_pk_mul_f32 v[114:115], v[30:31], v[18:19]
	v_pk_fma_f32 v[118:119], v[30:31], v[18:19], v[22:23]
	v_pk_mul_f32 v[4:5], v[4:5], v[24:25]
	v_pk_mul_f32 v[106:107], v[32:33], v[20:21]
	v_pk_mul_f32 v[24:25], v[100:101], v[24:25]
	ds_read_b128 v[98:101], v213 offset:18432
	v_cvt_pk_bf16_f32 v19, v106, v107
	ds_read_b128 v[106:109], v213 offset:19456
	v_pk_fma_f32 v[110:111], v[8:9], v[20:21], v[4:5]
	v_cvt_pk_bf16_f32 v5, v4, v5
	v_cvt_pk_bf16_f32 v3, v10, v11
	v_cvt_pk_bf16_f32 v4, v14, v15
	s_waitcnt lgkmcnt(0)
	v_pk_mul_f32 v[106:107], v[106:107], v[86:87]
	v_cvt_pk_bf16_f32 v2, v12, v13
	v_pk_mul_f32 v[120:121], v[98:99], v[82:83]
	v_pk_mul_f32 v[108:109], v[108:109], v[88:89]
	v_pk_fma_f32 v[98:99], v[98:99], v[82:83], v[106:107]
	v_mfma_f32_32x32x16_bf16 v[2:17], v[26:29], v[2:5], 0
	v_cvt_pk_bf16_f32 v18, v114, v115
	v_mul_f32_e32 v114, v100, v84
	v_mul_f32_e32 v115, v101, v85
	v_fma_f32 v100, v100, v84, v108
	v_fma_f32 v101, v101, v85, v109
	v_pk_add_f32 v[124:125], v[98:99], v[112:113]
	v_pk_add_f32 v[122:123], v[100:101], v[110:111]
	v_cvt_pk_bf16_f32 v101, v108, v109
	v_cvt_pk_bf16_f32 v100, v106, v107
	ds_read_b128 v[106:109], v213 offset:26624
	v_pk_fma_f32 v[116:117], v[32:33], v[20:21], v[24:25]
	v_cvt_pk_bf16_f32 v21, v24, v25
	v_cvt_pk_bf16_f32 v20, v22, v23
	ds_read_b128 v[110:113], v213 offset:27648
	v_cvt_pk_bf16_f32 v99, v114, v115
	v_mfma_f32_32x32x16_bf16 v[18:33], v[26:29], v[18:21], 0
	v_cvt_pk_bf16_f32 v98, v120, v121
	s_waitcnt lgkmcnt(1)
	v_mul_f32_e32 v114, v106, v82
	v_mul_f32_e32 v115, v107, v83
	s_waitcnt lgkmcnt(0)
	v_pk_mul_f32 v[86:87], v[110:111], v[86:87]
	v_pk_mul_f32 v[88:89], v[112:113], v[88:89]
	v_pk_fma_f32 v[82:83], v[106:107], v[82:83], v[86:87]
	v_mfma_f32_32x32x16_bf16 v[2:17], v[102:105], v[98:101], v[2:17]
	v_mul_f32_e32 v98, v108, v84
	v_mul_f32_e32 v99, v109, v85
	v_fma_f32 v84, v108, v84, v88
	v_fma_f32 v85, v109, v85, v89
	v_add_f32_e32 v108, v82, v118
	v_add_f32_e32 v109, v83, v119
	v_cvt_pk_bf16_f32 v83, v98, v99
	v_pk_add_f32 v[106:107], v[84:85], v[116:117]
	v_cvt_pk_bf16_f32 v85, v88, v89
	v_cvt_pk_bf16_f32 v84, v86, v87
	ds_read_b128 v[86:89], v213 offset:38912
	ds_read_b128 v[98:101], v213 offset:20480
	v_cvt_pk_bf16_f32 v82, v114, v115
	s_waitcnt lgkmcnt(0)
	v_pk_mul_f32 v[110:111], v[100:101], v[76:77]
	v_mfma_f32_32x32x16_bf16 v[18:33], v[102:105], v[82:85], v[18:33]
	ds_read_b128 v[82:85], v213 offset:21504
	ds_read_b128 v[102:105], v213 offset:28672
	v_mul_f32_e32 v112, v98, v74
	v_mul_f32_e32 v113, v99, v75
	s_waitcnt lgkmcnt(1)
	v_pk_mul_f32 v[84:85], v[84:85], v[80:81]
	v_pk_mul_f32 v[114:115], v[82:83], v[78:79]
	v_pk_fma_f32 v[82:83], v[100:101], v[76:77], v[84:85]
	v_cvt_pk_bf16_f32 v85, v84, v85
	v_pk_add_f32 v[116:117], v[82:83], v[122:123]
	v_cvt_pk_bf16_f32 v83, v110, v111
	v_cvt_pk_bf16_f32 v84, v114, v115
	v_cvt_pk_bf16_f32 v82, v112, v113
	v_pk_fma_f32 v[98:99], v[98:99], v[74:75], v[114:115]
	s_waitcnt lgkmcnt(0)
	v_pk_mul_f32 v[112:113], v[102:103], v[74:75]
	v_mfma_f32_32x32x16_bf16 v[2:17], v[86:89], v[82:85], v[2:17]
	ds_read_b128 v[82:85], v213 offset:29696
	v_add_f32_e32 v118, v98, v124
	v_add_f32_e32 v119, v99, v125
	v_mul_f32_e32 v110, v104, v76
	v_mul_f32_e32 v111, v105, v77
	ds_read_b128 v[98:101], v213 offset:39936
	s_waitcnt lgkmcnt(1)
	v_pk_mul_f32 v[78:79], v[82:83], v[78:79]
	v_pk_mul_f32 v[80:81], v[84:85], v[80:81]
	v_pk_fma_f32 v[74:75], v[102:103], v[74:75], v[78:79]
	v_pk_fma_f32 v[76:77], v[104:105], v[76:77], v[80:81]
	v_pk_add_f32 v[104:105], v[74:75], v[108:109]
	v_pk_add_f32 v[102:103], v[76:77], v[106:107]
	v_cvt_pk_bf16_f32 v77, v80, v81
	v_cvt_pk_bf16_f32 v76, v78, v79
	ds_read_b128 v[78:81], v213 offset:22528
	ds_read_b128 v[82:85], v213 offset:23552
	v_cvt_pk_bf16_f32 v75, v110, v111
	v_cvt_pk_bf16_f32 v74, v112, v113
	s_waitcnt lgkmcnt(0)
	v_pk_mul_f32 v[82:83], v[82:83], v[70:71]
	v_mfma_f32_32x32x16_bf16 v[18:33], v[86:89], v[74:77], v[18:33]
	v_mul_f32_e32 v74, v80, v68
	v_mul_f32_e32 v75, v81, v69
	v_mul_f32_e32 v76, v84, v72
	v_mul_f32_e32 v77, v85, v73
	v_mul_f32_e32 v86, v78, v66
	v_mul_f32_e32 v87, v79, v67
	v_pk_fma_f32 v[80:81], v[80:81], v[68:69], v[76:77]
	v_pk_fma_f32 v[78:79], v[78:79], v[66:67], v[82:83]
	v_cvt_pk_bf16_f32 v75, v74, v75
	v_pk_add_f32 v[88:89], v[80:81], v[116:117]
	v_pk_add_f32 v[106:107], v[78:79], v[118:119]
	ds_read_b128 v[78:81], v213 offset:30720
	v_cvt_pk_bf16_f32 v77, v76, v77
	v_cvt_pk_bf16_f32 v76, v82, v83
	ds_read_b128 v[82:85], v213 offset:31744
	v_cvt_pk_bf16_f32 v74, v86, v87
	s_waitcnt lgkmcnt(0)
	v_pk_mul_f32 v[72:73], v[84:85], v[72:73]
	v_mfma_f32_32x32x16_bf16 v[2:17], v[98:101], v[74:77], v[2:17]
	v_mul_f32_e32 v74, v80, v68
	v_mul_f32_e32 v75, v81, v69
	v_fma_f32 v68, v80, v68, v72
	v_fma_f32 v69, v81, v69, v73
	v_mul_f32_e32 v70, v82, v70
	v_mul_f32_e32 v71, v83, v71
	v_pk_add_f32 v[84:85], v[68:69], v[102:103]
	v_cvt_pk_bf16_f32 v69, v72, v73
	v_pk_mov_b32 v[72:73], v[96:97], v[94:95] op_sel:[1,0]
	v_mov_b32_e32 v97, v95
	v_pk_add_f32 v[72:73], v[72:73], v[96:97]
	v_pk_mul_f32 v[76:77], v[78:79], v[66:67]
	v_pk_fma_f32 v[66:67], v[78:79], v[66:67], v[70:71]
	v_pk_add_f32 v[72:73], v[72:73], v[72:73] op_sel:[0,1] op_sel_hi:[1,0]
	v_pk_add_f32 v[86:87], v[66:67], v[104:105]
	v_mov_b32_e32 v66, v72
	s_nop 1
	v_permlane32_swap_b32_e32 v72, v66
	v_add_f32_e32 v66, v72, v66
	v_cvt_pk_bf16_f32 v67, v74, v75
	v_rcp_f32_e32 v74, v66
	v_cvt_pk_bf16_f32 v68, v70, v71
	v_cvt_pk_bf16_f32 v66, v76, v77
	v_pk_mul_f32 v[70:71], v[46:47], v[74:75] op_sel_hi:[1,0]
	s_nop 0
	v_mfma_f32_32x32x16_bf16 v[18:33], v[98:101], v[66:69], v[18:33]
	v_mul_f32_e32 v66, v42, v74
	v_mul_f32_e32 v67, v43, v74
	v_pk_mov_b32 v[42:43], v[92:93], v[90:91] op_sel:[1,0]
	v_mov_b32_e32 v93, v91
	v_pk_add_f32 v[42:43], v[42:43], v[92:93]
	v_pk_mul_f32 v[68:69], v[44:45], v[74:75] op_sel_hi:[1,0]
	v_pk_add_f32 v[42:43], v[42:43], v[42:43] op_sel:[0,1] op_sel_hi:[1,0]
	v_pk_mov_b32 v[44:45], v[106:107], v[88:89] op_sel:[1,0]
	v_mov_b32_e32 v43, v42
	s_nop 1
	v_permlane32_swap_b32_e32 v42, v43
	v_add_f32_e32 v42, v42, v43
	v_rcp_f32_e32 v42, v42
	v_mov_b32_e32 v107, v89
	v_pk_add_f32 v[44:45], v[44:45], v[106:107]
	v_pk_mul_f32 v[72:73], v[48:49], v[74:75] op_sel_hi:[1,0]
	v_pk_add_f32 v[44:45], v[44:45], v[44:45] op_sel:[0,1] op_sel_hi:[1,0]
	v_pk_mul_f32 v[36:37], v[36:37], v[74:75] op_sel_hi:[1,0]
	v_pk_mul_f32 v[38:39], v[38:39], v[74:75] op_sel_hi:[1,0]
	v_pk_mul_f32 v[40:41], v[40:41], v[74:75] op_sel_hi:[1,0]
	v_pk_mul_f32 v[34:35], v[34:35], v[74:75] op_sel_hi:[1,0]
	v_pk_mul_f32 v[74:75], v[58:59], v[42:43] op_sel_hi:[1,0]
	v_pk_mul_f32 v[78:79], v[60:61], v[42:43] op_sel_hi:[1,0]
	v_pk_mul_f32 v[80:81], v[62:63], v[42:43] op_sel_hi:[1,0]
	v_pk_mul_f32 v[82:83], v[64:65], v[42:43] op_sel_hi:[1,0]
	v_pk_mul_f32 v[92:93], v[52:53], v[42:43] op_sel_hi:[1,0]
	v_mov_b32_e32 v43, v44
	s_nop 1
	v_permlane32_swap_b32_e32 v44, v43
	v_add_f32_e32 v43, v44, v43
	v_rcp_f32_e32 v76, v43
	v_pk_mul_f32 v[96:97], v[54:55], v[42:43] op_sel_hi:[1,0]
	v_pk_mul_f32 v[94:95], v[56:57], v[42:43] op_sel_hi:[1,0]
	v_pk_mul_f32 v[98:99], v[50:51], v[42:43] op_sel_hi:[1,0]
	v_pk_mul_f32 v[100:101], v[4:5], v[76:77] op_sel_hi:[1,0]
	v_pk_mov_b32 v[4:5], v[86:87], v[84:85] op_sel:[1,0]
	v_mov_b32_e32 v87, v85
	v_pk_add_f32 v[4:5], v[4:5], v[86:87]
	v_pk_mul_f32 v[102:103], v[6:7], v[76:77] op_sel_hi:[1,0]
	v_pk_add_f32 v[104:105], v[4:5], v[4:5] op_sel:[0,1] op_sel_hi:[1,0]
	v_cvt_pk_bf16_f32 v7, v40, v41
	ds_read_b128 v[84:87], v150 offset:52224
	ds_read_b128 v[50:53], v150 offset:35840
	ds_read_b128 v[54:57], v150 offset:36864
	ds_read_b128 v[58:61], v150 offset:37888
	ds_read_b128 v[62:65], v150 offset:38912
	v_cvt_pk_bf16_f32 v6, v38, v39
	v_cvt_pk_bf16_f32 v5, v36, v37
	v_cvt_pk_bf16_f32 v4, v34, v35
	ds_read_b128 v[88:91], v150 offset:53248
	ds_read_b128 v[34:37], v150 offset:39936
	ds_read_b128 v[38:41], v150 offset:40960
	ds_read_b128 v[42:45], v150 offset:41984
	ds_read_b128 v[46:49], v150 offset:43008
	v_cvt_pk_bf16_f32 v95, v94, v95
	v_cvt_pk_bf16_f32 v94, v96, v97
	v_cvt_pk_bf16_f32 v93, v92, v93
	v_cvt_pk_bf16_f32 v92, v98, v99
	s_waitcnt lgkmcnt(5)
	v_mfma_f32_32x32x16_bf16 v[50:65], v[84:87], v[4:7], v[50:65]
	v_mul_f32_e32 v10, v10, v76
	v_mul_f32_e32 v11, v11, v76
	v_mul_f32_e32 v12, v12, v76
	v_mul_f32_e32 v13, v13, v76
	v_mul_f32_e32 v8, v8, v76
	v_mul_f32_e32 v9, v9, v76
	v_mov_b32_e32 v77, v104
	s_nop 1
	v_permlane32_swap_b32_e32 v104, v77
	v_cvt_pk_bf16_f32 v73, v72, v73
	s_waitcnt lgkmcnt(0)
	v_mfma_f32_32x32x16_bf16 v[34:49], v[84:87], v[92:95], v[34:49]
	v_cvt_pk_bf16_f32 v72, v70, v71
	v_cvt_pk_bf16_f32 v70, v66, v67
	v_add_f32_e32 v66, v104, v77
	v_cvt_pk_bf16_f32 v71, v68, v69
	v_rcp_f32_e32 v104, v66
	v_cvt_pk_bf16_f32 v69, v82, v83
	v_cvt_pk_bf16_f32 v68, v80, v81
	v_cvt_pk_bf16_f32 v67, v78, v79
	v_cvt_pk_bf16_f32 v66, v74, v75
	ds_read_b128 v[78:81], v150 offset:54272
	v_mfma_f32_32x32x16_bf16 v[50:65], v[88:91], v[70:73], v[50:65]
	v_mul_f32_e32 v2, v2, v76
	v_mul_f32_e32 v3, v3, v76
	v_mul_f32_e32 v20, v20, v104
	v_mul_f32_e32 v21, v21, v104
	v_cvt_pk_bf16_f32 v85, v8, v9
	v_cvt_pk_bf16_f32 v82, v2, v3
	v_pk_mul_f32 v[2:3], v[22:23], v[104:105] op_sel_hi:[1,0]
	v_pk_mul_f32 v[8:9], v[24:25], v[104:105] op_sel_hi:[1,0]
	v_pk_mul_f32 v[18:19], v[18:19], v[104:105] op_sel_hi:[1,0]
	v_mfma_f32_32x32x16_bf16 v[34:49], v[88:91], v[66:69], v[34:49]
	v_cvt_pk_bf16_f32 v84, v102, v103
	v_cvt_pk_bf16_f32 v83, v100, v101
	ds_read_b128 v[86:89], v150 offset:55296
	v_cvt_pk_bf16_f32 v99, v8, v9
	v_cvt_pk_bf16_f32 v98, v2, v3
	v_cvt_pk_bf16_f32 v97, v20, v21
	v_cvt_pk_bf16_f32 v96, v18, v19
	s_waitcnt lgkmcnt(1)
	v_mfma_f32_32x32x16_bf16 v[50:65], v[78:81], v[82:85], v[50:65]
	v_mul_f32_e32 v2, v14, v76
	v_mul_f32_e32 v3, v15, v76
	v_mul_f32_e32 v8, v16, v76
	v_mul_f32_e32 v9, v17, v76
	v_mul_f32_e32 v14, v26, v104
	v_mul_f32_e32 v15, v27, v104
	v_cvt_pk_bf16_f32 v77, v8, v9
	v_cvt_pk_bf16_f32 v76, v2, v3
	v_cvt_pk_bf16_f32 v74, v10, v11
	v_pk_mul_f32 v[2:3], v[28:29], v[104:105] op_sel_hi:[1,0]
	v_mfma_f32_32x32x16_bf16 v[34:49], v[78:81], v[96:99], v[34:49]
	v_mul_f32_e32 v8, v30, v104
	v_mul_f32_e32 v9, v31, v104
	v_mul_f32_e32 v10, v32, v104
	v_mul_f32_e32 v11, v33, v104
	v_cvt_pk_bf16_f32 v75, v12, v13
	v_cvt_pk_bf16_f32 v81, v10, v11
	v_cvt_pk_bf16_f32 v80, v8, v9
	v_cvt_pk_bf16_f32 v79, v2, v3
	v_cvt_pk_bf16_f32 v78, v14, v15
	s_waitcnt lgkmcnt(0)
	v_mfma_f32_32x32x16_bf16 v[50:65], v[86:89], v[74:77], v[50:65]
	v_mfma_f32_32x32x16_bf16 v[34:49], v[86:89], v[78:81], v[34:49]
	ds_read_b128 v[86:89], v150 offset:56320
	ds_read_b128 v[18:21], v150 offset:44032
	ds_read_b128 v[22:25], v150 offset:45056
	ds_read_b128 v[26:29], v150 offset:46080
	ds_read_b128 v[30:33], v150 offset:47104
	ds_read_b128 v[100:103], v150 offset:57344
	s_waitcnt lgkmcnt(1)
	v_mfma_f32_32x32x16_bf16 v[18:33], v[86:89], v[4:7], v[18:33]
	ds_read_b128 v[2:5], v150 offset:48128
	ds_read_b128 v[6:9], v150 offset:49152
	ds_read_b128 v[10:13], v150 offset:50176
	ds_read_b128 v[14:17], v150 offset:51200
	s_waitcnt lgkmcnt(0)
	v_mfma_f32_32x32x16_bf16 v[2:17], v[86:89], v[92:95], v[2:17]
	v_mfma_f32_32x32x16_bf16 v[18:33], v[100:103], v[70:73], v[18:33]
	v_mfma_f32_32x32x16_bf16 v[2:17], v[100:103], v[66:69], v[2:17]
	ds_read_b128 v[66:69], v150 offset:58368
	ds_read_b128 v[70:73], v150 offset:59392
	s_waitcnt lgkmcnt(1)
	v_mfma_f32_32x32x16_bf16 v[18:33], v[66:69], v[82:85], v[18:33]
	v_mfma_f32_32x32x16_bf16 v[2:17], v[66:69], v[96:99], v[2:17]
	s_waitcnt lgkmcnt(0)
	v_mfma_f32_32x32x16_bf16 v[18:33], v[70:73], v[74:77], v[18:33]
	v_mfma_f32_32x32x16_bf16 v[2:17], v[70:73], v[78:81], v[2:17]
	s_nop 10
	v_mul_f32_e32 v66, v22, v22
	v_mul_f32_e32 v67, v23, v23
	v_mul_f32_e32 v68, v30, v30
	v_mul_f32_e32 v69, v31, v31
	v_mul_f32_e32 v70, v24, v24
	v_mul_f32_e32 v71, v25, v25
	v_pk_mul_f32 v[72:73], v[32:33], v[32:33]
	v_pk_mul_f32 v[74:75], v[20:21], v[20:21]
	v_pk_mul_f32 v[76:77], v[28:29], v[28:29]
	v_pk_mul_f32 v[78:79], v[26:27], v[26:27]
	v_pk_mul_f32 v[80:81], v[18:19], v[18:19]
	v_pk_fma_f32 v[78:79], v[58:59], v[58:59], v[78:79]
	v_pk_fma_f32 v[76:77], v[60:61], v[60:61], v[76:77]
	v_pk_fma_f32 v[74:75], v[52:53], v[52:53], v[74:75]
	v_pk_fma_f32 v[72:73], v[64:65], v[64:65], v[72:73]
	v_pk_fma_f32 v[70:71], v[56:57], v[56:57], v[70:71]
	v_pk_fma_f32 v[68:69], v[62:63], v[62:63], v[68:69]
	v_pk_fma_f32 v[66:67], v[54:55], v[54:55], v[66:67]
	v_pk_fma_f32 v[80:81], v[50:51], v[50:51], v[80:81]
	v_pk_add_f32 v[66:67], v[66:67], v[68:69]
	v_pk_add_f32 v[68:69], v[70:71], v[72:73]
	v_pk_add_f32 v[70:71], v[74:75], v[76:77]
	v_pk_add_f32 v[72:73], v[80:81], v[78:79]
	v_pk_add_f32 v[68:69], v[70:71], v[68:69]
	v_pk_add_f32 v[66:67], v[72:73], v[66:67]
	v_pk_mul_f32 v[72:73], v[14:15], v[14:15]
	v_pk_mov_b32 v[70:71], v[66:67], v[68:69] op_sel:[1,0]
	v_mov_b32_e32 v67, v69
	v_pk_add_f32 v[66:67], v[70:71], v[66:67]
	v_pk_mul_f32 v[70:71], v[6:7], v[6:7]
	v_pk_mul_f32 v[74:75], v[8:9], v[8:9]
	v_pk_mul_f32 v[76:77], v[16:17], v[16:17]
	v_pk_mul_f32 v[78:79], v[4:5], v[4:5]
	v_pk_mul_f32 v[80:81], v[12:13], v[12:13]
	v_pk_mul_f32 v[82:83], v[10:11], v[10:11]
	v_pk_mul_f32 v[84:85], v[2:3], v[2:3]
	v_pk_fma_f32 v[82:83], v[42:43], v[42:43], v[82:83]
	v_pk_fma_f32 v[80:81], v[44:45], v[44:45], v[80:81]
	v_pk_fma_f32 v[78:79], v[36:37], v[36:37], v[78:79]
	v_pk_fma_f32 v[76:77], v[48:49], v[48:49], v[76:77]
	v_pk_fma_f32 v[74:75], v[40:41], v[40:41], v[74:75]
	v_pk_fma_f32 v[72:73], v[46:47], v[46:47], v[72:73]
	v_pk_fma_f32 v[70:71], v[38:39], v[38:39], v[70:71]
	v_pk_fma_f32 v[84:85], v[34:35], v[34:35], v[84:85]
	v_pk_add_f32 v[70:71], v[70:71], v[72:73]
	v_pk_add_f32 v[72:73], v[74:75], v[76:77]
	v_pk_add_f32 v[74:75], v[78:79], v[80:81]
	v_pk_add_f32 v[76:77], v[84:85], v[82:83]
	v_pk_add_f32 v[72:73], v[74:75], v[72:73]
	v_pk_add_f32 v[70:71], v[76:77], v[70:71]
	v_pk_add_f32 v[66:67], v[66:67], v[66:67] op_sel:[0,1] op_sel_hi:[1,0]
	v_pk_mov_b32 v[74:75], v[70:71], v[72:73] op_sel:[1,0]
	v_mov_b32_e32 v71, v73
	v_pk_add_f32 v[70:71], v[74:75], v[70:71]
	v_mov_b32_e32 v69, v66
	v_pk_add_f32 v[70:71], v[70:71], v[70:71] op_sel:[0,1] op_sel_hi:[1,0]
	s_nop 0
	v_permlane32_swap_b32_e32 v66, v69
	v_mov_b32_e32 v68, v70
	s_nop 1
	v_permlane32_swap_b32_e32 v70, v68
	v_mov_b32_e32 v71, v66
	v_pk_add_f32 v[66:67], v[70:71], v[68:69]
	v_pk_fma_f32 v[66:67], v[66:67], s[0:1], v[152:153] op_sel_hi:[1,0,0]
	s_mov_b32 s1, 0x800000
	v_mul_f32_e32 v68, 0x4b800000, v67
	v_cmp_gt_f32_e32 vcc, s1, v67
	s_nop 1
	v_cndmask_b32_e32 v67, v67, v68, vcc
	v_rsq_f32_e32 v67, v67
	s_nop 0
	v_mul_f32_e32 v68, 0x45800000, v67
	v_cndmask_b32_e32 v68, v67, v68, vcc
	v_pk_mul_f32 v[158:159], v[50:51], v[68:69] op_sel_hi:[1,0]
	v_pk_mul_f32 v[50:51], v[18:19], v[68:69] op_sel_hi:[1,0]
	v_mul_f32_e32 v18, 0x4b800000, v66
	v_cmp_gt_f32_e32 vcc, s1, v66
	v_pk_mul_f32 v[80:81], v[60:61], v[68:69] op_sel_hi:[1,0]
	v_pk_mul_f32 v[60:61], v[28:29], v[68:69] op_sel_hi:[1,0]
	v_cndmask_b32_e32 v18, v66, v18, vcc
	v_rsq_f32_e32 v18, v18
	v_pk_mul_f32 v[78:79], v[58:59], v[68:69] op_sel_hi:[1,0]
	v_pk_mul_f32 v[160:161], v[52:53], v[68:69] op_sel_hi:[1,0]
	v_pk_mul_f32 v[82:83], v[54:55], v[68:69] op_sel_hi:[1,0]
	v_mul_f32_e32 v19, 0x45800000, v18
	v_cndmask_b32_e32 v28, v18, v19, vcc
	v_pk_mul_f32 v[168:169], v[56:57], v[68:69] op_sel_hi:[1,0]
	v_pk_mul_f32 v[58:59], v[26:27], v[68:69] op_sel_hi:[1,0]
	v_pk_mul_f32 v[52:53], v[20:21], v[68:69] op_sel_hi:[1,0]
	v_pk_mul_f32 v[54:55], v[22:23], v[68:69] op_sel_hi:[1,0]
	v_pk_mul_f32 v[56:57], v[24:25], v[68:69] op_sel_hi:[1,0]
	v_pk_mul_f32 v[18:19], v[42:43], v[28:29] op_sel_hi:[1,0]
	v_pk_mul_f32 v[20:21], v[44:45], v[28:29] op_sel_hi:[1,0]
	v_pk_mul_f32 v[22:23], v[46:47], v[28:29] op_sel_hi:[1,0]
	v_pk_mul_f32 v[26:27], v[48:49], v[28:29] op_sel_hi:[1,0]
	v_pk_mul_f32 v[162:163], v[34:35], v[28:29] op_sel_hi:[1,0]
	v_pk_mul_f32 v[164:165], v[36:37], v[28:29] op_sel_hi:[1,0]
	v_pk_mul_f32 v[166:167], v[38:39], v[28:29] op_sel_hi:[1,0]
	v_pk_mul_f32 v[24:25], v[40:41], v[28:29] op_sel_hi:[1,0]
	v_pk_mul_f32 v[104:105], v[2:3], v[28:29] op_sel_hi:[1,0]
	v_pk_mul_f32 v[112:113], v[4:5], v[28:29] op_sel_hi:[1,0]
	ds_read_b128 v[2:5], v150 offset:60416
	ds_read_b128 v[34:37], v174 offset:32768
	ds_read_b128 v[38:41], v174 offset:32800
	ds_read_b128 v[42:45], v174 offset:32832
	ds_read_b128 v[46:49], v174 offset:32864
	v_cvt_pk_bf16_f32 v129, v168, v169
	v_cvt_pk_bf16_f32 v128, v82, v83
	v_cvt_pk_bf16_f32 v127, v160, v161
	v_cvt_pk_bf16_f32 v126, v158, v159
	v_cvt_pk_bf16_f32 v137, v24, v25
	v_cvt_pk_bf16_f32 v136, v166, v167
	v_cvt_pk_bf16_f32 v135, v164, v165
	s_waitcnt lgkmcnt(0)
	v_mfma_f32_32x32x16_bf16 v[86:101], v[2:5], v[126:129], v[34:49]
	v_cvt_pk_bf16_f32 v134, v162, v163
	v_mul_f32_e32 v84, v62, v68
	v_mul_f32_e32 v85, v63, v68
	v_mul_f32_e32 v170, v64, v68
	v_mul_f32_e32 v171, v65, v68
	v_pk_mul_f32 v[62:63], v[30:31], v[68:69] op_sel_hi:[1,0]
	v_pk_mul_f32 v[64:65], v[32:33], v[68:69] op_sel_hi:[1,0]
	v_pk_mul_f32 v[116:117], v[6:7], v[28:29] op_sel_hi:[1,0]
	v_pk_mul_f32 v[154:155], v[8:9], v[28:29] op_sel_hi:[1,0]
	v_mfma_f32_32x32x16_bf16 v[34:49], v[2:5], v[134:137], v[34:49]
	ds_read_b128 v[6:9], v150 offset:61440
	ds_read_b128 v[66:69], v174 offset:32896
	ds_read_b128 v[106:109], v150 offset:64512
	v_cvt_pk_bf16_f32 v125, v170, v171
	v_cvt_pk_bf16_f32 v124, v84, v85
	v_cvt_pk_bf16_f32 v123, v80, v81
	v_cvt_pk_bf16_f32 v122, v78, v79
	v_cvt_pk_bf16_f32 v149, v26, v27
	v_cvt_pk_bf16_f32 v148, v22, v23
	v_cvt_pk_bf16_f32 v147, v20, v21
	v_cvt_pk_bf16_f32 v146, v18, v19
	s_waitcnt lgkmcnt(2)
	v_mfma_f32_32x32x16_bf16 v[86:101], v[6:9], v[122:125], v[86:101]
	v_mul_f32_e32 v102, v10, v28
	v_mul_f32_e32 v103, v11, v28
	v_mul_f32_e32 v110, v12, v28
	v_mul_f32_e32 v111, v13, v28
	v_mul_f32_e32 v114, v14, v28
	v_mul_f32_e32 v115, v15, v28
	v_pk_mul_f32 v[156:157], v[16:17], v[28:29] op_sel_hi:[1,0]
	ds_read_b128 v[176:179], v174 offset:33536
	ds_read_b128 v[180:183], v174 offset:33568
	ds_read_b128 v[184:187], v174 offset:33600
	ds_read_b128 v[28:31], v174 offset:33632
	ds_read_b128 v[188:191], v174 offset:33792
	ds_read_b128 v[192:195], v174 offset:33824
	ds_read_b128 v[196:199], v174 offset:33856
	ds_read_b128 v[200:203], v174 offset:33888
	ds_read_b128 v[204:207], v150 offset:62464
	v_cvt_pk_bf16_f32 v133, v56, v57
	v_mfma_f32_32x32x16_bf16 v[34:49], v[6:9], v[146:149], v[34:49]
	v_cvt_pk_bf16_f32 v132, v54, v55
	v_cvt_pk_bf16_f32 v131, v52, v53
	v_cvt_pk_bf16_f32 v130, v50, v51
	ds_read_b128 v[70:73], v174 offset:33664
	ds_read_b128 v[74:77], v174 offset:33920
	ds_read_b128 v[208:211], v150 offset:63488
	v_cvt_pk_bf16_f32 v145, v154, v155
	v_cvt_pk_bf16_f32 v144, v116, v117
	v_cvt_pk_bf16_f32 v143, v112, v113
	v_cvt_pk_bf16_f32 v142, v104, v105
	s_waitcnt lgkmcnt(3)
	v_mfma_f32_32x32x16_bf16 v[86:101], v[204:207], v[130:133], v[86:101]
	v_cvt_pk_bf16_f32 v121, v64, v65
	v_cvt_pk_bf16_f32 v120, v62, v63
	v_cvt_pk_bf16_f32 v119, v60, v61
	v_cvt_pk_bf16_f32 v118, v58, v59
	v_cvt_pk_bf16_f32 v141, v156, v157
	v_cvt_pk_bf16_f32 v140, v114, v115
	v_cvt_pk_bf16_f32 v139, v110, v111
	v_mfma_f32_32x32x16_bf16 v[34:49], v[204:207], v[142:145], v[34:49]
	v_cvt_pk_bf16_f32 v138, v102, v103
	v_fma_f32 v16, v30, v170, v202
	v_fma_f32 v17, v31, v171, v203
	v_fma_f32 v14, v28, v84, v200
	v_fma_f32 v15, v29, v85, v201
	v_pk_fma_f32 v[12:13], v[186:187], v[80:81], v[198:199]
	v_pk_fma_f32 v[10:11], v[184:185], v[78:79], v[196:197]
	v_pk_fma_f32 v[8:9], v[182:183], v[168:169], v[194:195]
	s_waitcnt lgkmcnt(0)
	v_mfma_f32_32x32x16_bf16 v[86:101], v[208:211], v[118:121], v[86:101]
	v_fma_f32 v6, v180, v82, v192
	v_fma_f32 v7, v181, v83, v193
	ds_read_b128 v[78:81], v174 offset:33760
	ds_read_b128 v[82:85], v174 offset:33248
	v_fma_f32 v4, v178, v160, v190
	v_fma_f32 v5, v179, v161, v191
	v_pk_fma_f32 v[2:3], v[176:177], v[158:159], v[188:189]
	v_pk_fma_f32 v[32:33], v[30:31], v[26:27], v[202:203]
	v_pk_fma_f32 v[30:31], v[28:29], v[22:23], v[200:201]
	v_pk_fma_f32 v[28:29], v[186:187], v[20:21], v[198:199]
	v_pk_fma_f32 v[26:27], v[184:185], v[18:19], v[196:197]
	v_pk_fma_f32 v[24:25], v[182:183], v[24:25], v[194:195]
	v_pk_fma_f32 v[22:23], v[180:181], v[166:167], v[192:193]
	v_pk_fma_f32 v[20:21], v[178:179], v[164:165], v[190:191]
	v_pk_fma_f32 v[18:19], v[176:177], v[162:163], v[188:189]
	ds_read_b128 v[158:161], v174 offset:33696
	ds_read_b128 v[162:165], v174 offset:33728
	ds_read_b128 v[166:169], v174 offset:33952
	ds_read_b128 v[176:179], v174 offset:33984
	ds_read_b128 v[180:183], v174 offset:34016
	ds_read_b128 v[184:187], v212 offset:11264
	v_mfma_f32_32x32x16_bf16 v[34:49], v[208:211], v[138:141], v[34:49]
	v_cvt_pk_bf16_f32 v86, v86, v87
	v_cvt_pk_bf16_f32 v87, v88, v89
	v_cvt_pk_bf16_f32 v88, v90, v91
	v_cvt_pk_bf16_f32 v89, v92, v93
	ds_read_b128 v[90:93], v212 offset:12288
	v_pk_max_i16 v86, v86, 0
	v_pk_max_i16 v87, v87, 0
	v_pk_max_i16 v88, v88, 0
	v_pk_max_i16 v89, v89, 0
	s_nop 1
	s_nop 0
	v_cvt_pk_bf16_f32 v188, v34, v35
	v_cvt_pk_bf16_f32 v189, v36, v37
	v_cvt_pk_bf16_f32 v190, v38, v39
	v_cvt_pk_bf16_f32 v191, v40, v41
	s_waitcnt lgkmcnt(1)
	v_mfma_f32_32x32x16_bf16 v[2:17], v[184:187], v[86:89], v[2:17]
	v_pk_max_i16 v188, v188, 0
	v_pk_max_i16 v189, v189, 0
	v_pk_max_i16 v190, v190, 0
	v_pk_max_i16 v191, v191, 0
	v_cvt_pk_bf16_f32 v94, v94, v95
	v_cvt_pk_bf16_f32 v95, v96, v97
	v_cvt_pk_bf16_f32 v96, v98, v99
	v_cvt_pk_bf16_f32 v97, v100, v101
	v_cvt_pk_bf16_f32 v98, v42, v43
	v_cvt_pk_bf16_f32 v99, v44, v45
	v_mfma_f32_32x32x16_bf16 v[18:33], v[184:187], v[188:191], v[18:33]
	ds_read_b128 v[184:187], v212 offset:19456
	v_cvt_pk_bf16_f32 v100, v46, v47
	v_cvt_pk_bf16_f32 v101, v48, v49
	v_fma_f32 v64, v80, v64, v182
	v_fma_f32 v65, v81, v65, v183
	v_pk_fma_f32 v[62:63], v[78:79], v[62:63], v[180:181]
	v_pk_fma_f32 v[60:61], v[164:165], v[60:61], v[178:179]
	v_pk_fma_f32 v[58:59], v[162:163], v[58:59], v[176:177]
	v_pk_max_i16 v94, v94, 0
	v_pk_max_i16 v95, v95, 0
	v_pk_max_i16 v96, v96, 0
	v_pk_max_i16 v97, v97, 0
	v_pk_max_i16 v98, v98, 0
	v_pk_max_i16 v99, v99, 0
	v_pk_max_i16 v100, v100, 0
	v_pk_max_i16 v101, v101, 0
	v_pk_fma_f32 v[56:57], v[160:161], v[56:57], v[168:169]
	s_waitcnt lgkmcnt(1)
	v_mfma_f32_32x32x16_bf16 v[2:17], v[90:93], v[94:97], v[2:17]
	v_fma_f32 v54, v158, v54, v166
	v_fma_f32 v55, v159, v55, v167
	v_fma_f32 v52, v72, v52, v76
	v_fma_f32 v53, v73, v53, v77
	v_fma_f32 v50, v70, v50, v74
	v_fma_f32 v51, v71, v51, v75
	v_pk_fma_f32 v[48:49], v[80:81], v[156:157], v[182:183]
	v_pk_fma_f32 v[46:47], v[78:79], v[114:115], v[180:181]
	v_pk_fma_f32 v[44:45], v[164:165], v[110:111], v[178:179]
	v_pk_fma_f32 v[42:43], v[162:163], v[102:103], v[176:177]
	v_mfma_f32_32x32x16_bf16 v[18:33], v[90:93], v[98:101], v[18:33]
	ds_read_b128 v[90:93], v212 offset:20480
	v_fma_f32 v40, v160, v154, v168
	v_fma_f32 v41, v161, v155, v169
	v_fma_f32 v38, v158, v116, v166
	v_fma_f32 v39, v159, v117, v167
	v_pk_fma_f32 v[36:37], v[72:73], v[112:113], v[76:77]
	v_pk_fma_f32 v[34:35], v[70:71], v[104:105], v[74:75]
	s_waitcnt lgkmcnt(1)
	v_mfma_f32_32x32x16_bf16 v[50:65], v[184:187], v[86:89], v[50:65]
	ds_read_b128 v[70:73], v174 offset:32928
	ds_read_b128 v[74:77], v174 offset:32960
	ds_read_b128 v[78:81], v174 offset:32992
	ds_read_b128 v[86:89], v174 offset:33024
	ds_read_b128 v[110:113], v212 offset:1024
	v_mfma_f32_32x32x16_bf16 v[34:49], v[184:187], v[188:191], v[34:49]
	s_waitcnt lgkmcnt(5)
	v_mfma_f32_32x32x16_bf16 v[50:65], v[90:93], v[94:97], v[50:65]
	v_mfma_f32_32x32x16_bf16 v[34:49], v[90:93], v[98:101], v[34:49]
	s_waitcnt lgkmcnt(2)
	v_mfma_f32_32x32x16_bf16 v[90:105], v[106:109], v[126:129], v[66:81]
	v_mfma_f32_32x32x16_bf16 v[66:81], v[106:109], v[134:137], v[66:81]
	ds_read_b128 v[106:109], v212 offset:0
	s_waitcnt lgkmcnt(0)
	v_mfma_f32_32x32x16_bf16 v[90:105], v[106:109], v[122:125], v[90:105]
	v_mfma_f32_32x32x16_bf16 v[66:81], v[106:109], v[146:149], v[66:81]
	ds_read_b128 v[106:109], v212 offset:2048
	v_mfma_f32_32x32x16_bf16 v[90:105], v[110:113], v[130:133], v[90:105]
	v_mfma_f32_32x32x16_bf16 v[66:81], v[110:113], v[142:145], v[66:81]
	ds_read_b128 v[110:113], v212 offset:13312
	s_waitcnt lgkmcnt(1)
	v_mfma_f32_32x32x16_bf16 v[90:105], v[106:109], v[118:121], v[90:105]
	v_mfma_f32_32x32x16_bf16 v[66:81], v[106:109], v[138:141], v[66:81]
	s_nop 10
	v_cvt_pk_bf16_f32 v90, v90, v91
	v_cvt_pk_bf16_f32 v91, v92, v93
	v_cvt_pk_bf16_f32 v92, v94, v95
	v_cvt_pk_bf16_f32 v94, v98, v99
	v_cvt_pk_bf16_f32 v95, v100, v101
	ds_read_b128 v[98:101], v212 offset:21504
	v_cvt_pk_bf16_f32 v66, v66, v67
	v_cvt_pk_bf16_f32 v67, v68, v69
	v_cvt_pk_bf16_f32 v68, v70, v71
	v_cvt_pk_bf16_f32 v93, v96, v97
	v_cvt_pk_bf16_f32 v69, v72, v73
	ds_read_b128 v[70:73], v212 offset:14336
	v_pk_max_i16 v90, v90, 0
	v_pk_max_i16 v91, v91, 0
	v_pk_max_i16 v92, v92, 0
	v_pk_max_i16 v93, v93, 0
	v_pk_max_i16 v66, v66, 0
	v_pk_max_i16 v67, v67, 0
	v_pk_max_i16 v68, v68, 0
	v_pk_max_i16 v69, v69, 0
	v_cvt_pk_bf16_f32 v96, v102, v103
	s_waitcnt lgkmcnt(2)
	v_mfma_f32_32x32x16_bf16 v[2:17], v[110:113], v[90:93], v[2:17]
	v_cvt_pk_bf16_f32 v97, v104, v105
	v_cvt_pk_bf16_f32 v74, v74, v75
	v_cvt_pk_bf16_f32 v75, v76, v77
	v_cvt_pk_bf16_f32 v76, v78, v79
	v_cvt_pk_bf16_f32 v77, v80, v81
	v_pk_max_i16 v94, v94, 0
	v_pk_max_i16 v95, v95, 0
	v_pk_max_i16 v96, v96, 0
	v_pk_max_i16 v97, v97, 0
	v_pk_max_i16 v74, v74, 0
	v_pk_max_i16 v75, v75, 0
	v_pk_max_i16 v76, v76, 0
	v_pk_max_i16 v77, v77, 0
	v_mfma_f32_32x32x16_bf16 v[18:33], v[110:113], v[66:69], v[18:33]
	s_waitcnt lgkmcnt(1)
	v_mfma_f32_32x32x16_bf16 v[34:49], v[98:101], v[66:69], v[34:49]
	ds_read_b128 v[66:69], v212 offset:22528
	v_mfma_f32_32x32x16_bf16 v[50:65], v[98:101], v[90:93], v[50:65]
	s_waitcnt lgkmcnt(1)
	v_mfma_f32_32x32x16_bf16 v[2:17], v[70:73], v[94:97], v[2:17]
	v_mfma_f32_32x32x16_bf16 v[18:33], v[70:73], v[74:77], v[18:33]
	ds_read_b128 v[78:81], v212 offset:3072
	s_waitcnt lgkmcnt(1)
	v_mfma_f32_32x32x16_bf16 v[50:65], v[66:69], v[94:97], v[50:65]
	ds_read_b128 v[90:93], v174 offset:33056
	ds_read_b128 v[94:97], v174 offset:33088
	ds_read_b128 v[98:101], v174 offset:33120
	ds_read_b128 v[70:73], v174 offset:33152
	v_mfma_f32_32x32x16_bf16 v[34:49], v[66:69], v[74:77], v[34:49]
	ds_read_b128 v[66:69], v212 offset:4096
	ds_read_b128 v[74:77], v212 offset:5120
	s_waitcnt lgkmcnt(3)
	v_mfma_f32_32x32x16_bf16 v[102:117], v[78:81], v[126:129], v[86:101]
	v_mfma_f32_32x32x16_bf16 v[86:101], v[78:81], v[134:137], v[86:101]
	s_waitcnt lgkmcnt(1)
	v_mfma_f32_32x32x16_bf16 v[86:101], v[66:69], v[146:149], v[86:101]
	v_mfma_f32_32x32x16_bf16 v[102:117], v[66:69], v[122:125], v[102:117]
	ds_read_b128 v[66:69], v212 offset:6144
	s_waitcnt lgkmcnt(1)
	v_mfma_f32_32x32x16_bf16 v[86:101], v[74:77], v[142:145], v[86:101]
	v_mfma_f32_32x32x16_bf16 v[102:117], v[74:77], v[130:133], v[102:117]
	ds_read_b128 v[74:77], v212 offset:15360
	s_waitcnt lgkmcnt(1)
	v_mfma_f32_32x32x16_bf16 v[86:101], v[66:69], v[138:141], v[86:101]
	v_mfma_f32_32x32x16_bf16 v[102:117], v[66:69], v[118:121], v[102:117]
	s_nop 10
	v_cvt_pk_bf16_f32 v78, v86, v87
	v_cvt_pk_bf16_f32 v80, v90, v91
	v_cvt_pk_bf16_f32 v79, v88, v89
	v_cvt_pk_bf16_f32 v81, v92, v93
	ds_read_b128 v[86:89], v212 offset:16384
	ds_read_b128 v[90:93], v212 offset:23552
	v_cvt_pk_bf16_f32 v66, v102, v103
	v_cvt_pk_bf16_f32 v67, v104, v105
	v_cvt_pk_bf16_f32 v68, v106, v107
	v_cvt_pk_bf16_f32 v69, v108, v109
	v_pk_max_i16 v66, v66, 0
	v_pk_max_i16 v67, v67, 0
	v_pk_max_i16 v68, v68, 0
	v_pk_max_i16 v69, v69, 0
	v_pk_max_i16 v78, v78, 0
	v_pk_max_i16 v79, v79, 0
	v_pk_max_i16 v80, v80, 0
	v_pk_max_i16 v81, v81, 0
	v_cvt_pk_bf16_f32 v94, v94, v95
	s_waitcnt lgkmcnt(2)
	v_mfma_f32_32x32x16_bf16 v[18:33], v[74:77], v[78:81], v[18:33]
	v_cvt_pk_bf16_f32 v95, v96, v97
	v_cvt_pk_bf16_f32 v96, v98, v99
	v_cvt_pk_bf16_f32 v97, v100, v101
	v_pk_max_i16 v94, v94, 0
	v_pk_max_i16 v95, v95, 0
	v_pk_max_i16 v96, v96, 0
	v_pk_max_i16 v97, v97, 0
	v_mfma_f32_32x32x16_bf16 v[2:17], v[74:77], v[66:69], v[2:17]
	v_cvt_pk_bf16_f32 v74, v110, v111
	v_cvt_pk_bf16_f32 v75, v112, v113
	v_cvt_pk_bf16_f32 v76, v114, v115
	v_cvt_pk_bf16_f32 v77, v116, v117
	v_pk_max_i16 v74, v74, 0
	v_pk_max_i16 v75, v75, 0
	v_pk_max_i16 v76, v76, 0
	v_pk_max_i16 v77, v77, 0
	s_waitcnt lgkmcnt(0)
	v_mfma_f32_32x32x16_bf16 v[50:65], v[90:93], v[66:69], v[50:65]
	ds_read_b128 v[66:69], v212 offset:24576
	v_mfma_f32_32x32x16_bf16 v[34:49], v[90:93], v[78:81], v[34:49]
	ds_read_b128 v[102:105], v212 offset:7168
	v_mfma_f32_32x32x16_bf16 v[2:17], v[86:89], v[74:77], v[2:17]
	s_waitcnt lgkmcnt(1)
	v_mfma_f32_32x32x16_bf16 v[50:65], v[66:69], v[74:77], v[50:65]
	ds_read_b128 v[74:77], v174 offset:33184
	ds_read_b128 v[78:81], v174 offset:33216
	v_mfma_f32_32x32x16_bf16 v[34:49], v[66:69], v[94:97], v[34:49]
	ds_read_b128 v[66:69], v212 offset:8192
	v_mfma_f32_32x32x16_bf16 v[18:33], v[86:89], v[94:97], v[18:33]
	s_waitcnt lgkmcnt(1)
	v_mfma_f32_32x32x16_bf16 v[86:101], v[102:105], v[126:129], v[70:85]
	v_mfma_f32_32x32x16_bf16 v[70:85], v[102:105], v[134:137], v[70:85]
	ds_read_b128 v[102:105], v212 offset:9216
	v_lshlrev_b32_e32 v135, 2, v1
	v_add_u32_e32 v134, v172, v174
	s_waitcnt lgkmcnt(1)
	v_mfma_f32_32x32x16_bf16 v[86:101], v[66:69], v[122:125], v[86:101]
	v_mfma_f32_32x32x16_bf16 v[70:85], v[66:69], v[146:149], v[70:85]
	ds_read_b128 v[66:69], v212 offset:10240
	s_waitcnt lgkmcnt(1)
	v_mfma_f32_32x32x16_bf16 v[86:101], v[102:105], v[130:133], v[86:101]
	v_mfma_f32_32x32x16_bf16 v[70:85], v[102:105], v[142:145], v[70:85]
	ds_read_b128 v[102:105], v212 offset:17408
	s_waitcnt lgkmcnt(1)
	v_mfma_f32_32x32x16_bf16 v[86:101], v[66:69], v[118:121], v[86:101]
	v_mfma_f32_32x32x16_bf16 v[70:85], v[66:69], v[138:141], v[70:85]
	s_nop 10
	v_cvt_pk_bf16_f32 v68, v90, v91
	v_cvt_pk_bf16_f32 v69, v92, v93
	ds_read_b128 v[90:93], v212 offset:25600
	v_cvt_pk_bf16_f32 v66, v86, v87
	v_cvt_pk_bf16_f32 v67, v88, v89
	v_pk_max_i16 v66, v66, 0
	v_pk_max_i16 v67, v67, 0
	v_pk_max_i16 v68, v68, 0
	v_pk_max_i16 v69, v69, 0
	v_cvt_pk_bf16_f32 v70, v70, v71
	v_cvt_pk_bf16_f32 v71, v72, v73
	s_waitcnt lgkmcnt(1)
	v_mfma_f32_32x32x16_bf16 v[2:17], v[102:105], v[66:69], v[2:17]
	v_cvt_pk_bf16_f32 v72, v74, v75
	v_cvt_pk_bf16_f32 v73, v76, v77
	ds_read_b128 v[74:77], v212 offset:18432
	v_cvt_pk_bf16_f32 v86, v94, v95
	v_cvt_pk_bf16_f32 v87, v96, v97
	v_cvt_pk_bf16_f32 v88, v98, v99
	s_waitcnt lgkmcnt(1)
	v_mfma_f32_32x32x16_bf16 v[50:65], v[90:93], v[66:69], v[50:65]
	ds_read_b128 v[66:69], v212 offset:26624
	v_cvt_pk_bf16_f32 v89, v100, v101
	v_pk_max_i16 v86, v86, 0
	v_pk_max_i16 v87, v87, 0
	v_pk_max_i16 v88, v88, 0
	v_pk_max_i16 v89, v89, 0
	v_pk_max_i16 v70, v70, 0
	v_pk_max_i16 v71, v71, 0
	v_pk_max_i16 v72, v72, 0
	v_pk_max_i16 v73, v73, 0
	v_cvt_pk_bf16_f32 v78, v78, v79
	v_cvt_pk_bf16_f32 v79, v80, v81
	s_waitcnt lgkmcnt(1)
	v_mfma_f32_32x32x16_bf16 v[2:17], v[74:77], v[86:89], v[2:17]
	v_cvt_pk_bf16_f32 v80, v82, v83
	v_cvt_pk_bf16_f32 v81, v84, v85
	v_pk_max_i16 v78, v78, 0
	v_pk_max_i16 v79, v79, 0
	v_pk_max_i16 v80, v80, 0
	v_pk_max_i16 v81, v81, 0
	s_waitcnt lgkmcnt(0)
	v_mfma_f32_32x32x16_bf16 v[50:65], v[66:69], v[86:89], v[50:65]
	v_mfma_f32_32x32x16_bf16 v[34:49], v[90:93], v[70:73], v[34:49]
	s_nop 10
	v_add_f32_e32 v130, v10, v58
	v_add_f32_e32 v131, v11, v59
	v_add_f32_e32 v132, v12, v60
	v_add_f32_e32 v133, v13, v61
	v_add_f32_e32 v138, v4, v52
	v_add_f32_e32 v139, v5, v53
	v_pk_add_f32 v[140:141], v[16:17], v[64:65]
	v_pk_add_f32 v[142:143], v[8:9], v[56:57]
	v_pk_add_f32 v[144:145], v[14:15], v[62:63]
	v_pk_add_f32 v[146:147], v[6:7], v[54:55]
	v_mfma_f32_32x32x16_bf16 v[18:33], v[102:105], v[70:73], v[18:33]
	ds_read2st64_b32 v[70:71], v135 offset0:133 offset1:134
	v_add_f32_e32 v148, v2, v50
	v_add_f32_e32 v149, v3, v51
	v_add_f32_e32 v144, v146, v144
	v_add_f32_e32 v145, v147, v145
	v_pk_add_f32 v[140:141], v[142:143], v[140:141]
	v_pk_add_f32 v[132:133], v[138:139], v[132:133]
	v_pk_add_f32 v[130:131], v[148:149], v[130:131]
	v_pk_add_f32 v[132:133], v[132:133], v[140:141]
	v_pk_add_f32 v[130:131], v[130:131], v[144:145]
	v_mfma_f32_32x32x16_bf16 v[34:49], v[66:69], v[78:81], v[34:49]
	v_pk_mov_b32 v[138:139], v[130:131], v[132:133] op_sel:[1,0]
	v_mov_b32_e32 v131, v133
	s_waitcnt vmcnt(0) lgkmcnt(0)
	v_mul_f32_e32 v66, v175, v70
	v_pk_add_f32 v[130:131], v[138:139], v[130:131]
	ds_write_b32 v173, v66 offset:512
	v_mul_f32_e32 v66, v175, v71
	v_pk_add_f32 v[130:131], v[130:131], v[130:131] op_sel:[0,1] op_sel_hi:[1,0]
	s_waitcnt lgkmcnt(0)
	ds_read_b128 v[102:105], v174 offset:34560
	ds_read_b128 v[98:101], v174 offset:34592
	ds_read_b128 v[110:113], v174 offset:34624
	ds_read_b128 v[106:109], v174 offset:34656
	ds_read_b128 v[114:117], v174 offset:34688
	ds_read_b128 v[122:125], v174 offset:34720
	ds_read_b128 v[118:121], v174 offset:34752
	ds_read_b128 v[126:129], v174 offset:34784
	v_mov_b32_dpp v66, v66 quad_perm:[1,0,3,2] row_mask:0xf bank_mask:0xf bound_ctrl:1
	v_mov_b32_e32 v131, v130
	v_fmac_f32_e32 v66, v175, v71
	s_nop 0
	v_permlane32_swap_b32_e32 v130, v131
	v_add_f32_dpp v66, v66, v66 quad_perm:[2,3,0,1] row_mask:0xf bank_mask:0xf bound_ctrl:1
	v_add_f32_e32 v130, v130, v131
	v_fmamk_f32 v65, v130, 0xbc800000, v65
	v_add_f32_dpp v66, v66, v66 row_half_mirror row_mask:0xf bank_mask:0xf bound_ctrl:1
	v_fmamk_f32 v64, v130, 0xbc800000, v64
	v_fmamk_f32 v63, v130, 0xbc800000, v63
	v_fmamk_f32 v62, v130, 0xbc800000, v62
	v_fmamk_f32 v61, v130, 0xbc800000, v61
	v_fmamk_f32 v60, v130, 0xbc800000, v60
	v_fmamk_f32 v59, v130, 0xbc800000, v59
	v_fmamk_f32 v58, v130, 0xbc800000, v58
	v_fmamk_f32 v57, v130, 0xbc800000, v57
	v_fmamk_f32 v56, v130, 0xbc800000, v56
	v_fmamk_f32 v55, v130, 0xbc800000, v55
	v_fmamk_f32 v54, v130, 0xbc800000, v54
	v_fmamk_f32 v53, v130, 0xbc800000, v53
	v_fmamk_f32 v52, v130, 0xbc800000, v52
	v_fmamk_f32 v51, v130, 0xbc800000, v51
	v_fmac_f32_e32 v50, 0xbc800000, v130
	v_add_f32_dpp v66, v66, v66 row_ror:8 row_mask:0xf bank_mask:0xf bound_ctrl:1
	v_fmamk_f32 v17, v130, 0xbc800000, v17
	v_fmamk_f32 v16, v130, 0xbc800000, v16
	v_fmamk_f32 v15, v130, 0xbc800000, v15
	v_fmamk_f32 v14, v130, 0xbc800000, v14
	v_fmamk_f32 v13, v130, 0xbc800000, v13
	v_fmamk_f32 v12, v130, 0xbc800000, v12
	v_fmamk_f32 v11, v130, 0xbc800000, v11
	v_fmamk_f32 v10, v130, 0xbc800000, v10
	v_fmamk_f32 v9, v130, 0xbc800000, v9
	v_fmamk_f32 v8, v130, 0xbc800000, v8
	v_fmamk_f32 v7, v130, 0xbc800000, v7
	v_fmamk_f32 v6, v130, 0xbc800000, v6
	v_fmamk_f32 v5, v130, 0xbc800000, v5
	v_fmamk_f32 v4, v130, 0xbc800000, v4
	v_fmamk_f32 v3, v130, 0xbc800000, v3
	v_fmac_f32_e32 v2, 0xbc800000, v130
	v_pk_mul_f32 v[130:131], v[54:55], v[54:55]
	v_pk_mul_f32 v[132:133], v[62:63], v[62:63]
	v_pk_mul_f32 v[138:139], v[50:51], v[50:51]
	v_pk_mul_f32 v[140:141], v[58:59], v[58:59]
	v_pk_mul_f32 v[142:143], v[56:57], v[56:57]
	v_pk_mul_f32 v[144:145], v[64:65], v[64:65]
	v_pk_mul_f32 v[146:147], v[52:53], v[52:53]
	v_pk_mul_f32 v[148:149], v[60:61], v[60:61]
	v_mov_b32_e32 v67, v66
	v_pk_fma_f32 v[148:149], v[12:13], v[12:13], v[148:149]
	v_pk_fma_f32 v[146:147], v[4:5], v[4:5], v[146:147]
	v_pk_fma_f32 v[144:145], v[16:17], v[16:17], v[144:145]
	v_pk_fma_f32 v[142:143], v[8:9], v[8:9], v[142:143]
	v_pk_fma_f32 v[140:141], v[10:11], v[10:11], v[140:141]
	v_pk_fma_f32 v[138:139], v[2:3], v[2:3], v[138:139]
	v_pk_fma_f32 v[132:133], v[14:15], v[14:15], v[132:133]
	v_pk_fma_f32 v[130:131], v[6:7], v[6:7], v[130:131]
	v_permlane16_swap_b32_e32 v66, v67
	v_pk_add_f32 v[130:131], v[130:131], v[132:133]
	v_pk_add_f32 v[132:133], v[138:139], v[140:141]
	v_pk_add_f32 v[138:139], v[142:143], v[144:145]
	v_pk_add_f32 v[140:141], v[146:147], v[148:149]
	v_mfma_f32_32x32x16_bf16 v[18:33], v[74:77], v[78:81], v[18:33]
	v_add_f32_e32 v136, v66, v67
	ds_read_b128 v[70:73], v134 offset:512
	ds_read_b128 v[66:69], v134 offset:544
	ds_read_b128 v[78:81], v134 offset:576
	ds_read_b128 v[74:77], v134 offset:608
	ds_read_b128 v[82:85], v134 offset:640
	ds_read_b128 v[90:93], v134 offset:672
	ds_read_b128 v[86:89], v134 offset:704
	ds_read_b128 v[94:97], v134 offset:736
	v_pk_add_f32 v[138:139], v[140:141], v[138:139]
	v_pk_add_f32 v[130:131], v[132:133], v[130:131]
	s_waitcnt lgkmcnt(8)
	v_pk_mul_f32 v[140:141], v[126:127], v[62:63]
	v_pk_mov_b32 v[132:133], v[130:131], v[138:139] op_sel:[1,0]
	v_mov_b32_e32 v131, v139
	v_pk_mul_f32 v[138:139], v[122:123], v[54:55]
	v_pk_mul_f32 v[142:143], v[114:115], v[50:51]
	v_pk_mul_f32 v[144:145], v[118:119], v[58:59]
	v_pk_mul_f32 v[146:147], v[124:125], v[56:57]
	v_pk_mul_f32 v[148:149], v[128:129], v[64:65]
	v_pk_mul_f32 v[154:155], v[116:117], v[52:53]
	v_pk_mul_f32 v[156:157], v[120:121], v[60:61]
	v_pk_fma_f32 v[154:155], v[104:105], v[4:5], v[154:155]
	v_pk_fma_f32 v[156:157], v[112:113], v[12:13], v[156:157]
	v_pk_fma_f32 v[148:149], v[108:109], v[16:17], v[148:149]
	v_pk_fma_f32 v[146:147], v[100:101], v[8:9], v[146:147]
	v_pk_fma_f32 v[144:145], v[110:111], v[10:11], v[144:145]
	v_pk_fma_f32 v[142:143], v[102:103], v[2:3], v[142:143]
	v_pk_fma_f32 v[140:141], v[106:107], v[14:15], v[140:141]
	v_pk_fma_f32 v[138:139], v[98:99], v[6:7], v[138:139]
	v_pk_add_f32 v[130:131], v[132:133], v[130:131]
	v_pk_add_f32 v[138:139], v[138:139], v[140:141]
	v_pk_add_f32 v[140:141], v[142:143], v[144:145]
	v_pk_add_f32 v[142:143], v[146:147], v[148:149]
	v_pk_add_f32 v[144:145], v[154:155], v[156:157]
	v_pk_add_f32 v[132:133], v[130:131], v[130:131] op_sel:[0,1] op_sel_hi:[1,0]
	v_pk_add_f32 v[142:143], v[144:145], v[142:143]
	v_pk_add_f32 v[138:139], v[140:141], v[138:139]
	v_add_f32_e32 v133, v142, v143
	v_add_f32_e32 v130, v138, v139
	s_waitcnt lgkmcnt(2)
	v_pk_mul_f32 v[138:139], v[90:91], v[54:55]
	s_waitcnt lgkmcnt(0)
	v_pk_mul_f32 v[140:141], v[94:95], v[62:63]
	v_pk_mul_f32 v[142:143], v[82:83], v[50:51]
	v_pk_mul_f32 v[144:145], v[86:87], v[58:59]
	v_pk_mul_f32 v[146:147], v[92:93], v[56:57]
	v_pk_mul_f32 v[148:149], v[96:97], v[64:65]
	v_pk_mul_f32 v[154:155], v[84:85], v[52:53]
	v_pk_mul_f32 v[156:157], v[88:89], v[60:61]
	v_add_f32_e32 v130, v130, v133
	v_pk_fma_f32 v[156:157], v[80:81], v[12:13], v[156:157]
	v_pk_fma_f32 v[154:155], v[72:73], v[4:5], v[154:155]
	v_pk_fma_f32 v[148:149], v[76:77], v[16:17], v[148:149]
	v_pk_fma_f32 v[146:147], v[68:69], v[8:9], v[146:147]
	v_pk_fma_f32 v[144:145], v[78:79], v[10:11], v[144:145]
	v_pk_fma_f32 v[142:143], v[70:71], v[2:3], v[142:143]
	v_pk_fma_f32 v[140:141], v[74:75], v[14:15], v[140:141]
	v_pk_fma_f32 v[138:139], v[66:67], v[6:7], v[138:139]
	v_mov_b32_e32 v133, v130
	v_pk_add_f32 v[138:139], v[138:139], v[140:141]
	v_pk_add_f32 v[140:141], v[142:143], v[144:145]
	v_pk_add_f32 v[142:143], v[146:147], v[148:149]
	v_pk_add_f32 v[144:145], v[154:155], v[156:157]
	v_permlane32_swap_b32_e32 v130, v133
	v_pk_add_f32 v[142:143], v[144:145], v[142:143]
	v_add_f32_e32 v160, v130, v133
	v_pk_add_f32 v[138:139], v[140:141], v[138:139]
	v_add_f32_e32 v133, v142, v143
	v_pk_add_f32 v[140:141], v[26:27], v[42:43]
	v_pk_add_f32 v[142:143], v[28:29], v[44:45]
	v_pk_add_f32 v[144:145], v[20:21], v[36:37]
	v_pk_add_f32 v[146:147], v[32:33], v[48:49]
	v_pk_add_f32 v[148:149], v[24:25], v[40:41]
	v_pk_add_f32 v[154:155], v[30:31], v[46:47]
	v_pk_add_f32 v[156:157], v[22:23], v[38:39]
	v_pk_add_f32 v[158:159], v[18:19], v[34:35]
	v_pk_add_f32 v[154:155], v[156:157], v[154:155]
	v_pk_add_f32 v[146:147], v[148:149], v[146:147]
	v_pk_add_f32 v[142:143], v[144:145], v[142:143]
	v_pk_add_f32 v[140:141], v[158:159], v[140:141]
	v_pk_add_f32 v[142:143], v[142:143], v[146:147]
	v_pk_add_f32 v[140:141], v[140:141], v[154:155]
	v_add_f32_e32 v130, v138, v139
	v_pk_mov_b32 v[144:145], v[140:141], v[142:143] op_sel:[1,0]
	v_mov_b32_e32 v141, v143
	v_pk_add_f32 v[140:141], v[144:145], v[140:141]
	v_add_f32_e32 v133, v130, v133
	v_pk_add_f32 v[140:141], v[140:141], v[140:141] op_sel:[0,1] op_sel_hi:[1,0]
	v_mov_b32_e32 v131, v132
	v_mov_b32_e32 v130, v140
	s_nop 1
	v_permlane32_swap_b32_e32 v140, v130
	v_add_f32_e32 v130, v140, v130
	v_fmamk_f32 v49, v130, 0xbc800000, v49
	v_fmamk_f32 v48, v130, 0xbc800000, v48
	v_fmamk_f32 v47, v130, 0xbc800000, v47
	v_fmamk_f32 v46, v130, 0xbc800000, v46
	v_fmamk_f32 v45, v130, 0xbc800000, v45
	v_fmamk_f32 v44, v130, 0xbc800000, v44
	v_fmamk_f32 v43, v130, 0xbc800000, v43
	v_fmamk_f32 v42, v130, 0xbc800000, v42
	v_fmamk_f32 v41, v130, 0xbc800000, v41
	v_fmamk_f32 v40, v130, 0xbc800000, v40
	v_fmamk_f32 v39, v130, 0xbc800000, v39
	v_fmamk_f32 v38, v130, 0xbc800000, v38
	v_fmamk_f32 v37, v130, 0xbc800000, v37
	v_fmamk_f32 v36, v130, 0xbc800000, v36
	v_fmamk_f32 v35, v130, 0xbc800000, v35
	v_fmac_f32_e32 v34, 0xbc800000, v130
	v_fmamk_f32 v33, v130, 0xbc800000, v33
	v_fmamk_f32 v32, v130, 0xbc800000, v32
	v_fmamk_f32 v31, v130, 0xbc800000, v31
	v_fmamk_f32 v30, v130, 0xbc800000, v30
	v_fmamk_f32 v29, v130, 0xbc800000, v29
	v_fmamk_f32 v28, v130, 0xbc800000, v28
	v_fmamk_f32 v27, v130, 0xbc800000, v27
	v_fmamk_f32 v26, v130, 0xbc800000, v26
	v_fmamk_f32 v25, v130, 0xbc800000, v25
	v_fmamk_f32 v24, v130, 0xbc800000, v24
	v_fmamk_f32 v23, v130, 0xbc800000, v23
	v_fmamk_f32 v22, v130, 0xbc800000, v22
	v_fmamk_f32 v21, v130, 0xbc800000, v21
	v_fmamk_f32 v20, v130, 0xbc800000, v20
	v_fmamk_f32 v19, v130, 0xbc800000, v19
	v_fmac_f32_e32 v18, 0xbc800000, v130
	v_pk_mul_f32 v[140:141], v[38:39], v[38:39]
	v_pk_mul_f32 v[142:143], v[46:47], v[46:47]
	v_pk_mul_f32 v[144:145], v[34:35], v[34:35]
	v_pk_mul_f32 v[146:147], v[42:43], v[42:43]
	v_pk_mul_f32 v[148:149], v[40:41], v[40:41]
	v_pk_mul_f32 v[154:155], v[48:49], v[48:49]
	v_pk_mul_f32 v[156:157], v[36:37], v[36:37]
	v_pk_mul_f32 v[158:159], v[44:45], v[44:45]
	v_pk_fma_f32 v[156:157], v[20:21], v[20:21], v[156:157]
	v_pk_fma_f32 v[158:159], v[28:29], v[28:29], v[158:159]
	v_pk_fma_f32 v[154:155], v[32:33], v[32:33], v[154:155]
	v_pk_fma_f32 v[148:149], v[24:25], v[24:25], v[148:149]
	v_pk_fma_f32 v[146:147], v[26:27], v[26:27], v[146:147]
	v_pk_fma_f32 v[144:145], v[18:19], v[18:19], v[144:145]
	v_pk_fma_f32 v[142:143], v[30:31], v[30:31], v[142:143]
	v_pk_fma_f32 v[140:141], v[22:23], v[22:23], v[140:141]
	v_permlane32_swap_b32_e32 v132, v131
	v_pk_add_f32 v[140:141], v[140:141], v[142:143]
	v_pk_add_f32 v[142:143], v[144:145], v[146:147]
	v_pk_add_f32 v[144:145], v[148:149], v[154:155]
	v_pk_add_f32 v[146:147], v[156:157], v[158:159]
	v_pk_add_f32 v[140:141], v[142:143], v[140:141]
	v_pk_add_f32 v[144:145], v[146:147], v[144:145]
	v_pk_mul_f32 v[122:123], v[122:123], v[38:39]
	v_pk_mov_b32 v[142:143], v[140:141], v[144:145] op_sel:[1,0]
	v_mov_b32_e32 v141, v145
	v_pk_add_f32 v[140:141], v[142:143], v[140:141]
	v_pk_mul_f32 v[126:127], v[126:127], v[46:47]
	v_pk_add_f32 v[140:141], v[140:141], v[140:141] op_sel:[0,1] op_sel_hi:[1,0]
	v_pk_mul_f32 v[114:115], v[114:115], v[34:35]
	v_mov_b32_e32 v130, v140
	s_nop 1
	v_permlane32_swap_b32_e32 v140, v130
	v_mov_b32_e32 v141, v132
	v_pk_add_f32 v[130:131], v[140:141], v[130:131]
	v_pk_mul_f32 v[118:119], v[118:119], v[42:43]
	v_pk_fma_f32 v[130:131], v[130:131], s[0:1], v[152:153] op_sel_hi:[1,0,0]
	v_pk_mul_f32 v[124:125], v[124:125], v[40:41]
	v_mul_f32_e32 v132, 0x4b800000, v131
	v_cmp_gt_f32_e32 vcc, s1, v131
	v_pk_mul_f32 v[128:129], v[128:129], v[48:49]
	v_pk_mul_f32 v[116:117], v[116:117], v[36:37]
	v_pk_mul_f32 v[120:121], v[120:121], v[44:45]
	v_cndmask_b32_e32 v131, v131, v132, vcc
	v_mul_f32_e32 v132, 0x4b800000, v130
	v_cmp_gt_f32_e64 s[0:1], s1, v130
	v_pk_fma_f32 v[112:113], v[112:113], v[28:29], v[120:121]
	v_pk_fma_f32 v[104:105], v[104:105], v[20:21], v[116:117]
	v_pk_fma_f32 v[108:109], v[108:109], v[32:33], v[128:129]
	v_pk_fma_f32 v[100:101], v[100:101], v[24:25], v[124:125]
	v_pk_fma_f32 v[110:111], v[110:111], v[26:27], v[118:119]
	v_pk_fma_f32 v[102:103], v[102:103], v[18:19], v[114:115]
	v_pk_fma_f32 v[106:107], v[106:107], v[30:31], v[126:127]
	v_pk_fma_f32 v[98:99], v[98:99], v[22:23], v[122:123]
	v_rsq_f32_e32 v131, v131
	v_cndmask_b32_e64 v130, v130, v132, s[0:1]
	v_pk_add_f32 v[98:99], v[98:99], v[106:107]
	v_pk_add_f32 v[102:103], v[102:103], v[110:111]
	v_pk_add_f32 v[100:101], v[100:101], v[108:109]
	v_pk_add_f32 v[104:105], v[104:105], v[112:113]
	v_rsq_f32_e32 v132, v130
	v_pk_add_f32 v[100:101], v[104:105], v[100:101]
	v_pk_add_f32 v[98:99], v[102:103], v[98:99]
	v_mul_f32_e32 v130, 0x45800000, v131
	v_add_f32_e32 v98, v98, v99
	v_add_f32_e32 v99, v100, v101
	v_add_f32_e32 v98, v98, v99
	v_mov_b32_e32 v99, v98
	v_pk_mul_f32 v[90:91], v[90:91], v[38:39]
	v_pk_mul_f32 v[94:95], v[94:95], v[46:47]
	v_pk_mul_f32 v[82:83], v[82:83], v[34:35]
	v_pk_mul_f32 v[86:87], v[86:87], v[42:43]
	v_cndmask_b32_e32 v130, v131, v130, vcc
	v_mul_f32_e32 v131, 0x45800000, v132
	v_permlane32_swap_b32_e32 v98, v99
	v_pk_fma_f32 v[78:79], v[78:79], v[26:27], v[86:87]
	v_pk_fma_f32 v[70:71], v[70:71], v[18:19], v[82:83]
	v_pk_fma_f32 v[74:75], v[74:75], v[30:31], v[94:95]
	v_pk_fma_f32 v[66:67], v[66:67], v[22:23], v[90:91]
	v_cndmask_b32_e64 v131, v132, v131, s[0:1]
	v_add_f32_e32 v98, v98, v99
	v_pk_add_f32 v[66:67], v[66:67], v[74:75]
	v_pk_add_f32 v[70:71], v[70:71], v[78:79]
	v_mul_f32_e32 v139, v160, v130
	v_mul_f32_e32 v98, v98, v131
	v_pk_add_f32 v[66:67], v[70:71], v[66:67]
	v_cmp_gt_u32_e32 vcc, 32, v1
	v_add_f32_e32 v66, v66, v67
	v_pk_mul_f32 v[92:93], v[92:93], v[40:41]
	v_cndmask_b32_e32 v67, v98, v139, vcc
	v_add_f32_e32 v67, s12, v67
	v_pk_mul_f32 v[96:97], v[96:97], v[48:49]
	v_pk_mul_f32 v[84:85], v[84:85], v[36:37]
	v_pk_mul_f32 v[88:89], v[88:89], v[44:45]
	v_mul_f32_e32 v67, 0xbfb8aa3b, v67
	v_pk_fma_f32 v[80:81], v[80:81], v[28:29], v[88:89]
	v_pk_fma_f32 v[72:73], v[72:73], v[20:21], v[84:85]
	v_pk_fma_f32 v[76:77], v[76:77], v[32:33], v[96:97]
	v_pk_fma_f32 v[68:69], v[68:69], v[24:25], v[92:93]
	v_exp_f32_e32 v70, v67
	v_pk_add_f32 v[68:69], v[68:69], v[76:77]
	v_pk_add_f32 v[72:73], v[72:73], v[80:81]
	v_cmp_lt_i32_e64 s[0:1], 0, v151
	v_pk_add_f32 v[68:69], v[72:73], v[68:69]
	v_mov_b32_e32 v137, v136
	v_add_f32_e32 v67, v68, v69
	v_add_f32_e32 v67, v66, v67
	v_add_f32_e32 v66, 1.0, v70
	v_rcp_f32_e32 v66, v66
	v_mov_b32_e32 v69, 0xff800000
	v_mov_b32_e32 v138, v133
	v_mov_b32_e32 v68, v67
	v_cndmask_b32_e64 v70, v69, v66, s[0:1]
	v_mbcnt_lo_u32_b32 v66, -1, 0
	v_mbcnt_hi_u32_b32 v66, -1, v66
	v_permlane32_swap_b32_e32 v136, v137
	v_permlane32_swap_b32_e32 v133, v138
	v_permlane32_swap_b32_e32 v67, v68
	v_and_b32_e32 v86, 64, v66
	s_mov_b32 s14, 8
	s_mov_b32 s13, 0
	v_mov_b32_e32 v66, 0
	s_waitcnt lgkmcnt(0)
